# speedup vs baseline: 1.0154x; 1.0052x over previous
.LBB0_40:
	s_cmpk_gt_i32 s2, 0x7f
	s_cbranch_scc1 .Lp_end
	s_waitcnt vmcnt(9)
	v_mov_b32_e32 v44, 0
	v_cmp_ne_u32_e64 s[46:47], 0, v17
	v_cmp_ne_u32_e64 s[48:49], 0, v16
	v_cmp_ne_u32_e64 s[50:51], 0, v15
	v_cmp_ne_u32_e64 s[52:53], 0, v14
	v_addc_co_u32_e64 v44, s[54:55], v44, v44, s[46:47]
	v_addc_co_u32_e64 v44, s[54:55], v44, v44, s[48:49]
	v_addc_co_u32_e64 v44, s[54:55], v44, v44, s[50:51]
	v_addc_co_u32_e64 v44, s[54:55], v44, v44, s[52:53]
	v_cmp_ne_u32_e64 s[46:47], 0, v13
	v_cmp_ne_u32_e64 s[48:49], 0, v12
	v_cmp_ne_u32_e64 s[50:51], 0, v11
	v_cmp_ne_u32_e64 s[52:53], 0, v10
	v_addc_co_u32_e64 v44, s[54:55], v44, v44, s[46:47]
	v_addc_co_u32_e64 v44, s[54:55], v44, v44, s[48:49]
	v_addc_co_u32_e64 v44, s[54:55], v44, v44, s[50:51]
	v_addc_co_u32_e64 v44, s[54:55], v44, v44, s[52:53]
	v_cmp_ne_u32_e64 s[46:47], 0, v9
	v_cmp_ne_u32_e64 s[48:49], 0, v8
	v_cmp_ne_u32_e64 s[50:51], 0, v7
	v_cmp_ne_u32_e64 s[52:53], 0, v6
	v_addc_co_u32_e64 v44, s[54:55], v44, v44, s[46:47]
	v_addc_co_u32_e64 v44, s[54:55], v44, v44, s[48:49]
	v_addc_co_u32_e64 v44, s[54:55], v44, v44, s[50:51]
	v_addc_co_u32_e64 v44, s[54:55], v44, v44, s[52:53]
	v_cmp_ne_u32_e64 s[46:47], 0, v5
	v_cmp_ne_u32_e64 s[48:49], 0, v4
	v_cmp_ne_u32_e64 s[50:51], 0, v3
	v_cmp_ne_u32_e64 s[52:53], 0, v2
	v_addc_co_u32_e64 v44, s[54:55], v44, v44, s[46:47]
	v_addc_co_u32_e64 v44, s[54:55], v44, v44, s[48:49]
	v_addc_co_u32_e64 v44, s[54:55], v44, v44, s[50:51]
	v_addc_co_u32_e64 v44, s[54:55], v44, v44, s[52:53]
	s_waitcnt vmcnt(5)
	v_mov_b32_e32 v45, 0
	v_cmp_ne_u32_e64 s[46:47], 0, v147
	v_cmp_ne_u32_e64 s[48:49], 0, v146
	v_cmp_ne_u32_e64 s[50:51], 0, v145
	v_cmp_ne_u32_e64 s[52:53], 0, v144
	v_addc_co_u32_e64 v45, s[54:55], v45, v45, s[46:47]
	v_addc_co_u32_e64 v45, s[54:55], v45, v45, s[48:49]
	v_addc_co_u32_e64 v45, s[54:55], v45, v45, s[50:51]
	v_addc_co_u32_e64 v45, s[54:55], v45, v45, s[52:53]
	v_cmp_ne_u32_e64 s[46:47], 0, v143
	v_cmp_ne_u32_e64 s[48:49], 0, v142
	v_cmp_ne_u32_e64 s[50:51], 0, v141
	v_cmp_ne_u32_e64 s[52:53], 0, v140
	v_addc_co_u32_e64 v45, s[54:55], v45, v45, s[46:47]
	v_addc_co_u32_e64 v45, s[54:55], v45, v45, s[48:49]
	v_addc_co_u32_e64 v45, s[54:55], v45, v45, s[50:51]
	v_addc_co_u32_e64 v45, s[54:55], v45, v45, s[52:53]
	v_cmp_ne_u32_e64 s[46:47], 0, v139
	v_cmp_ne_u32_e64 s[48:49], 0, v138
	v_cmp_ne_u32_e64 s[50:51], 0, v137
	v_cmp_ne_u32_e64 s[52:53], 0, v136
	v_addc_co_u32_e64 v45, s[54:55], v45, v45, s[46:47]
	v_addc_co_u32_e64 v45, s[54:55], v45, v45, s[48:49]
	v_addc_co_u32_e64 v45, s[54:55], v45, v45, s[50:51]
	v_addc_co_u32_e64 v45, s[54:55], v45, v45, s[52:53]
	v_cmp_ne_u32_e64 s[46:47], 0, v135
	v_cmp_ne_u32_e64 s[48:49], 0, v134
	v_cmp_ne_u32_e64 s[50:51], 0, v133
	v_cmp_ne_u32_e64 s[52:53], 0, v132
	v_addc_co_u32_e64 v45, s[54:55], v45, v45, s[46:47]
	v_addc_co_u32_e64 v45, s[54:55], v45, v45, s[48:49]
	v_addc_co_u32_e64 v45, s[54:55], v45, v45, s[50:51]
	v_addc_co_u32_e64 v45, s[54:55], v45, v45, s[52:53]
	s_lshl_b32 s13, s2, 4
	v_lshl_add_u32 v46, v128, 1, s13
	v_lshlrev_b32_e32 v46, 7, v46
	v_lshl_add_u32 v46, v126, 1, v46
	global_store_short v46, v44, s[36:37]
	global_store_short v46, v45, s[36:37] offset:128
